# MFMA-VALU interleave: silu of GEMM1 tiles 2-5 moved into the shadows of GEMM2 step-0/step-1 MFMAs (clean per-tile blocks, fresh temps)
# speedup vs baseline: 1.0022x; 1.0022x over previous
.LBB1_6:
	s_waitcnt vmcnt(14)
	ds_write_b128 v119, v[38:41]
	s_waitcnt vmcnt(13)
	ds_write_b128 v119, v[42:45] offset:2304
	s_waitcnt vmcnt(12)
	ds_write_b128 v119, v[46:49] offset:4608
	s_waitcnt vmcnt(11)
	ds_write_b128 v119, v[50:53] offset:6912
	ds_bpermute_b32 v42, v107, v64
	ds_bpermute_b32 v43, v109, v64
	ds_bpermute_b32 v44, v110, v64
	v_add_u32_e32 v0, 0x1000, v62
	ds_bpermute_b32 v50, v111, v64
	v_min_i32_e32 v0, 0x927b, v0
	v_lshl_or_b32 v40, v0, 4, v106
	s_waitcnt lgkmcnt(3)
	v_lshlrev_b32_e32 v0, 7, v42
	v_ashrrev_i32_e32 v65, 31, v64
	v_lshl_add_u64 v[46:47], v[98:99], 0, v[0:1]
	s_waitcnt lgkmcnt(2)
	v_lshlrev_b32_e32 v0, 7, v43
	v_lshl_add_u64 v[38:39], v[64:65], 2, v[96:97]
	v_ashrrev_i32_e32 v41, 31, v40
	v_lshl_add_u64 v[48:49], v[98:99], 0, v[0:1]
	s_waitcnt lgkmcnt(1)
	v_lshlrev_b32_e32 v0, 7, v44
	s_waitcnt vmcnt(10)
	ds_bpermute_b32 v68, v114, v108
	ds_bpermute_b32 v66, v115, v108
	global_load_dword v108, v[38:39], off
	v_lshl_add_u64 v[38:39], v[40:41], 2, v[94:95]
	v_lshl_add_u64 v[64:65], v[100:101], 0, v[0:1]
	s_waitcnt lgkmcnt(2)
	v_lshlrev_b32_e32 v0, 7, v50
	global_load_dword v135, v[38:39], off
	s_nop 0
	global_load_dwordx4 v[38:41], v[46:47], off
	global_load_dwordx4 v[42:45], v[48:49], off
	v_lshl_add_u64 v[70:71], v[100:101], 0, v[0:1]
	global_load_dwordx4 v[46:49], v[64:65], off
	global_load_dwordx4 v[50:53], v[70:71], off
	ds_read_b128 v[70:73], v120
	ds_read_b128 v[74:77], v120 offset:64
	ds_read_b128 v[78:81], v120 offset:4608
	ds_read_b128 v[82:85], v120 offset:4672
	v_add_u32_e32 v0, 0x800, v62
	ds_write_b128 v121, v[2:5]
	ds_write_b128 v121, v[6:9] offset:1088
	ds_write_b128 v121, v[10:13] offset:2176
	ds_write_b128 v121, v[14:17] offset:3264
	ds_write_b128 v121, v[18:21] offset:4352
	ds_write_b128 v121, v[22:25] offset:5440
	s_waitcnt vmcnt(15)
	ds_write_b128 v121, v[26:29] offset:6528
	s_waitcnt vmcnt(14)
	ds_write_b128 v121, v[30:33] offset:7616
	ds_write_b128 v122, v[34:37] offset:8704
	v_min_i32_e32 v2, 0x927b, v0
	v_ashrrev_i32_e32 v3, 31, v2
	v_lshlrev_b64 v[4:5], 13, v[2:3]
	v_lshlrev_b64 v[2:3], 10, v[2:3]
	v_lshl_add_u64 v[18:19], v[102:103], 0, v[4:5]
	v_lshl_add_u64 v[62:63], v[104:105], 0, v[2:3]
	v_add_co_u32_e32 v64, vcc, s3, v18
	global_load_dwordx4 v[2:5], v[18:19], off nt
	global_load_dwordx4 v[6:9], v[18:19], off offset:1024 nt
	global_load_dwordx4 v[10:13], v[18:19], off offset:2048 nt
	global_load_dwordx4 v[14:17], v[18:19], off offset:3072 nt
	v_addc_co_u32_e32 v65, vcc, 0, v19, vcc
	global_load_dwordx4 v[34:37], v[62:63], off nt
	global_load_dwordx4 v[18:21], v[64:65], off nt
	global_load_dwordx4 v[22:25], v[64:65], off offset:1024 nt
	global_load_dwordx4 v[26:29], v[64:65], off offset:2048 nt
	global_load_dwordx4 v[30:33], v[64:65], off offset:3072 nt
	s_waitcnt lgkmcnt(13)
	v_add_f32_e32 v67, v68, v66
	v_mul_f32_e32 v184, 0xc3000000, v67
	s_waitcnt lgkmcnt(12)
	v_cvt_f32_ubyte3_e32 v169, v70
	v_cvt_f32_ubyte2_e32 v168, v70
	v_cvt_f32_ubyte1_e32 v171, v70
	v_cvt_f32_ubyte0_e32 v170, v70
	ds_read_b128 v[62:65], v123
	ds_read_b128 v[86:89], v123 offset:64
	ds_read_b128 v[90:93], v112
	ds_read_b128 v[136:139], v112 offset:4608
	ds_read_b128 v[140:143], v112 offset:9216
	ds_read_b128 v[144:147], v112 offset:13824
	ds_read_b128 v[148:151], v112 offset:18432
	ds_read_b128 v[152:155], v112 offset:23040
	ds_read_b128 v[156:159], v112 offset:27648
	ds_read_b128 v[160:163], v112 offset:32256
	s_waitcnt lgkmcnt(14)
	v_cvt_f32_ubyte1_e32 v165, v78
	v_cvt_f32_ubyte0_e32 v164, v78
	v_cvt_f32_ubyte3_e32 v167, v78
	v_cvt_f32_ubyte2_e32 v166, v78
	v_pk_fma_f32 v[170:171], v[170:171], v[68:69], v[184:185] op_sel_hi:[1,0,0]
	v_pk_fma_f32 v[168:169], v[168:169], v[68:69], v[184:185] op_sel_hi:[1,0,0]
	v_pk_fma_f32 v[164:165], v[164:165], v[66:67], v[170:171] op_sel_hi:[1,0,1]
	v_pk_fma_f32 v[166:167], v[166:167], v[66:67], v[168:169] op_sel_hi:[1,0,1]
	v_cvt_f32_ubyte1_e32 v169, v79
	v_cvt_f32_ubyte0_e32 v168, v79
	v_cvt_f32_ubyte3_e32 v171, v79
	v_cvt_f32_ubyte2_e32 v170, v79
	v_cvt_f32_ubyte3_e32 v79, v71
	v_cvt_f32_ubyte2_e32 v78, v71
	v_cvt_f32_ubyte1_e32 v173, v71
	v_cvt_f32_ubyte0_e32 v172, v71
	v_pk_fma_f32 v[70:71], v[172:173], v[68:69], v[184:185] op_sel_hi:[1,0,0]
	v_pk_fma_f32 v[78:79], v[78:79], v[68:69], v[184:185] op_sel_hi:[1,0,0]
	v_cvt_f32_ubyte3_e32 v173, v72
	v_cvt_f32_ubyte2_e32 v172, v72
	v_cvt_f32_ubyte1_e32 v175, v72
	v_cvt_f32_ubyte0_e32 v174, v72
	v_pk_fma_f32 v[170:171], v[170:171], v[66:67], v[78:79] op_sel_hi:[1,0,1]
	v_pk_fma_f32 v[168:169], v[168:169], v[66:67], v[70:71] op_sel_hi:[1,0,1]
	v_cvt_f32_ubyte1_e32 v71, v80
	v_cvt_f32_ubyte0_e32 v70, v80
	v_cvt_f32_ubyte3_e32 v79, v80
	v_cvt_f32_ubyte2_e32 v78, v80
	v_pk_fma_f32 v[176:177], v[174:175], v[68:69], v[184:185] op_sel_hi:[1,0,0]
	v_pk_fma_f32 v[172:173], v[172:173], v[68:69], v[184:185] op_sel_hi:[1,0,0]
	v_cvt_f32_ubyte2_e32 v80, v73
	v_pk_fma_f32 v[174:175], v[78:79], v[66:67], v[172:173] op_sel_hi:[1,0,1]
	v_pk_fma_f32 v[172:173], v[70:71], v[66:67], v[176:177] op_sel_hi:[1,0,1]
	v_cvt_f32_ubyte1_e32 v177, v73
	v_cvt_f32_ubyte0_e32 v176, v73
	v_cvt_f32_ubyte1_e32 v71, v81
	v_cvt_f32_ubyte0_e32 v70, v81
	v_cvt_f32_ubyte3_e32 v79, v81
	v_cvt_f32_ubyte2_e32 v78, v81
	v_cvt_f32_ubyte3_e32 v81, v73
	v_pk_fma_f32 v[176:177], v[176:177], v[68:69], v[184:185] op_sel_hi:[1,0,0]
	v_pk_fma_f32 v[72:73], v[80:81], v[68:69], v[184:185] op_sel_hi:[1,0,0]
	v_pk_fma_f32 v[70:71], v[70:71], v[66:67], v[176:177] op_sel_hi:[1,0,1]
	v_cvt_f32_ubyte3_e32 v177, v74
	v_cvt_f32_ubyte2_e32 v176, v74
	v_cvt_f32_ubyte1_e32 v179, v74
	v_cvt_f32_ubyte0_e32 v178, v74
	v_pk_fma_f32 v[72:73], v[78:79], v[66:67], v[72:73] op_sel_hi:[1,0,1]
	v_cvt_f32_ubyte1_e32 v79, v82
	v_cvt_f32_ubyte0_e32 v78, v82
	v_cvt_f32_ubyte3_e32 v81, v82
	v_cvt_f32_ubyte2_e32 v80, v82
	v_pk_fma_f32 v[178:179], v[178:179], v[68:69], v[184:185] op_sel_hi:[1,0,0]
	v_pk_fma_f32 v[176:177], v[176:177], v[68:69], v[184:185] op_sel_hi:[1,0,0]
	v_pk_fma_f32 v[78:79], v[78:79], v[66:67], v[178:179] op_sel_hi:[1,0,1]
	v_pk_fma_f32 v[80:81], v[80:81], v[66:67], v[176:177] op_sel_hi:[1,0,1]
	v_cvt_f32_ubyte1_e32 v177, v83
	v_cvt_f32_ubyte0_e32 v176, v83
	v_cvt_f32_ubyte3_e32 v179, v83
	v_cvt_f32_ubyte2_e32 v178, v83
	v_cvt_f32_ubyte3_e32 v83, v75
	v_cvt_f32_ubyte2_e32 v82, v75
	v_cvt_f32_ubyte1_e32 v181, v75
	v_cvt_f32_ubyte0_e32 v180, v75
	v_pk_fma_f32 v[74:75], v[180:181], v[68:69], v[184:185] op_sel_hi:[1,0,0]
	v_pk_fma_f32 v[82:83], v[82:83], v[68:69], v[184:185] op_sel_hi:[1,0,0]
	v_cvt_f32_ubyte3_e32 v181, v76
	v_cvt_f32_ubyte2_e32 v180, v76
	v_cvt_f32_ubyte1_e32 v183, v76
	v_cvt_f32_ubyte0_e32 v182, v76
	v_pk_fma_f32 v[178:179], v[178:179], v[66:67], v[82:83] op_sel_hi:[1,0,1]
	v_pk_fma_f32 v[176:177], v[176:177], v[66:67], v[74:75] op_sel_hi:[1,0,1]
	v_cvt_f32_ubyte1_e32 v75, v84
	v_cvt_f32_ubyte0_e32 v74, v84
	v_cvt_f32_ubyte3_e32 v83, v84
	v_cvt_f32_ubyte2_e32 v82, v84
	v_pk_fma_f32 v[186:187], v[182:183], v[68:69], v[184:185] op_sel_hi:[1,0,0]
	v_pk_fma_f32 v[180:181], v[180:181], v[68:69], v[184:185] op_sel_hi:[1,0,0]
	v_cvt_f32_ubyte2_e32 v84, v77
	v_pk_fma_f32 v[182:183], v[82:83], v[66:67], v[180:181] op_sel_hi:[1,0,1]
	v_pk_fma_f32 v[180:181], v[74:75], v[66:67], v[186:187] op_sel_hi:[1,0,1]
	v_cvt_f32_ubyte1_e32 v75, v85
	v_cvt_f32_ubyte0_e32 v74, v85
	v_cvt_f32_ubyte3_e32 v83, v85
	v_cvt_f32_ubyte2_e32 v82, v85
	v_cvt_f32_ubyte3_e32 v85, v77
	v_cvt_f32_ubyte1_e32 v187, v77
	v_cvt_f32_ubyte0_e32 v186, v77
	v_pk_fma_f32 v[76:77], v[186:187], v[68:69], v[184:185] op_sel_hi:[1,0,0]
	v_pk_fma_f32 v[68:69], v[84:85], v[68:69], v[184:185] op_sel_hi:[1,0,0]
	s_nop 0
	v_pk_fma_f32 v[68:69], v[82:83], v[66:67], v[68:69] op_sel_hi:[1,0,1]
	v_pk_fma_f32 v[66:67], v[74:75], v[66:67], v[76:77] op_sel_hi:[1,0,1]
	ds_read_b128 v[74:77], v123 offset:128
	ds_read_b128 v[82:85], v123 offset:192
	ds_read_b128 v[184:187], v112 offset:64
	ds_read_b128 v[188:191], v112 offset:4672
	ds_read_b128 v[192:195], v112 offset:9280
	ds_read_b128 v[196:199], v112 offset:13888
	ds_read_b128 v[200:203], v112 offset:18496
	ds_read_b128 v[204:207], v112 offset:23104
	ds_read_b128 v[208:211], v112 offset:27712
	ds_read_b128 v[212:215], v112 offset:32320
	s_waitcnt lgkmcnt(14)
	v_cvt_pk_bf16_f32 v62, v62, v63
	v_cvt_pk_bf16_f32 v63, v64, v65
	v_cvt_pk_bf16_f32 v64, v86, v87
	v_cvt_pk_bf16_f32 v65, v88, v89
	s_nop 1
	v_mfma_f32_16x16x32_bf16 v[86:89], v[90:93], v[62:65], v[164:167]
	v_mfma_f32_16x16x32_bf16 v[90:93], v[136:139], v[62:65], v[168:171]
	v_mfma_f32_16x16x32_bf16 v[136:139], v[140:143], v[62:65], v[172:175]
	v_mfma_f32_16x16x32_bf16 v[70:73], v[144:147], v[62:65], v[70:73]
	s_waitcnt lgkmcnt(13)
	v_mfma_f32_16x16x32_bf16 v[78:81], v[148:151], v[62:65], v[78:81]
	s_waitcnt lgkmcnt(12)
	v_mfma_f32_16x16x32_bf16 v[140:143], v[152:155], v[62:65], v[176:179]
	s_waitcnt lgkmcnt(11)
	v_mfma_f32_16x16x32_bf16 v[144:147], v[156:159], v[62:65], v[180:183]
	s_waitcnt lgkmcnt(10)
	v_mfma_f32_16x16x32_bf16 v[62:65], v[160:163], v[62:65], v[66:69]
	s_nop 2
	ds_read_b128 v[66:69], v123 offset:256
	ds_read_b128 v[148:151], v123 offset:320
	ds_read_b128 v[152:155], v112 offset:128
	ds_read_b128 v[156:159], v112 offset:4736
	ds_read_b128 v[160:163], v112 offset:9344
	ds_read_b128 v[164:167], v112 offset:13952
	ds_read_b128 v[168:171], v112 offset:18560
	ds_read_b128 v[172:175], v112 offset:23168
	ds_read_b128 v[176:179], v112 offset:27776
	ds_read_b128 v[180:183], v112 offset:32384
	s_waitcnt lgkmcnt(14)
	v_cvt_pk_bf16_f32 v74, v74, v75
	v_cvt_pk_bf16_f32 v75, v76, v77
	v_cvt_pk_bf16_f32 v76, v82, v83
	v_cvt_pk_bf16_f32 v77, v84, v85
	s_waitcnt lgkmcnt(10)
	s_nop 0
	v_mfma_f32_16x16x32_bf16 v[62:65], v[212:215], v[74:77], v[62:65]
	v_mfma_f32_16x16x32_bf16 v[82:85], v[184:187], v[74:77], v[86:89]
	v_mfma_f32_16x16x32_bf16 v[86:89], v[188:191], v[74:77], v[90:93]
	v_mfma_f32_16x16x32_bf16 v[90:93], v[192:195], v[74:77], v[136:139]
	v_mfma_f32_16x16x32_bf16 v[70:73], v[196:199], v[74:77], v[70:73]
	v_mfma_f32_16x16x32_bf16 v[78:81], v[200:203], v[74:77], v[78:81]
	v_mfma_f32_16x16x32_bf16 v[136:139], v[204:207], v[74:77], v[140:143]
	v_mfma_f32_16x16x32_bf16 v[140:143], v[208:211], v[74:77], v[144:147]
	ds_read_b128 v[74:77], v123 offset:384
	s_nop 1
	ds_read_b128 v[144:147], v123 offset:448
	ds_read_b128 v[184:187], v112 offset:192
	ds_read_b128 v[188:191], v112 offset:4800
	ds_read_b128 v[192:195], v112 offset:9408
	ds_read_b128 v[196:199], v112 offset:14016
	ds_read_b128 v[200:203], v112 offset:18624
	ds_read_b128 v[204:207], v112 offset:23232
	ds_read_b128 v[208:211], v112 offset:27840
	ds_read_b128 v[212:215], v112 offset:32448
	s_waitcnt lgkmcnt(14)
	v_cvt_pk_bf16_f32 v66, v66, v67
	v_cvt_pk_bf16_f32 v67, v68, v69
	v_cvt_pk_bf16_f32 v68, v148, v149
	v_cvt_pk_bf16_f32 v69, v150, v151
	s_waitcnt lgkmcnt(10)
	s_nop 0
	v_mfma_f32_16x16x32_bf16 v[62:65], v[180:183], v[66:69], v[62:65]
	v_mfma_f32_16x16x32_bf16 v[82:85], v[152:155], v[66:69], v[82:85]
	v_mfma_f32_16x16x32_bf16 v[86:89], v[156:159], v[66:69], v[86:89]
	v_mfma_f32_16x16x32_bf16 v[90:93], v[160:163], v[66:69], v[90:93]
	v_mfma_f32_16x16x32_bf16 v[70:73], v[164:167], v[66:69], v[70:73]
	v_mfma_f32_16x16x32_bf16 v[78:81], v[168:171], v[66:69], v[78:81]
	v_mfma_f32_16x16x32_bf16 v[136:139], v[172:175], v[66:69], v[136:139]
	v_mfma_f32_16x16x32_bf16 v[140:143], v[176:179], v[66:69], v[140:143]
	ds_read2st64_b64 v[66:69], v134 offset0:54 offset1:63
	ds_read2st64_b64 v[148:151], v134 offset0:36 offset1:45
	ds_read2st64_b64 v[152:155], v134 offset0:18 offset1:27
	ds_read2st64_b64 v[156:159], v134 offset1:9
	ds_read_b128 v[160:163], v124 offset:8704
	s_waitcnt lgkmcnt(14)
	v_cvt_pk_bf16_f32 v74, v74, v75
	v_cvt_pk_bf16_f32 v75, v76, v77
	s_waitcnt lgkmcnt(13)
	v_cvt_pk_bf16_f32 v76, v144, v145
	v_cvt_pk_bf16_f32 v77, v146, v147
	s_waitcnt lgkmcnt(5)
	s_nop 0
	v_mfma_f32_16x16x32_bf16 v[62:65], v[212:215], v[74:77], v[62:65]
	v_mfma_f32_16x16x32_bf16 v[82:85], v[184:187], v[74:77], v[82:85]
	v_mfma_f32_16x16x32_bf16 v[86:89], v[188:191], v[74:77], v[86:89]
	v_mfma_f32_16x16x32_bf16 v[90:93], v[192:195], v[74:77], v[90:93]
	v_mfma_f32_16x16x32_bf16 v[70:73], v[196:199], v[74:77], v[70:73]
	v_mfma_f32_16x16x32_bf16 v[78:81], v[200:203], v[74:77], v[78:81]
	v_mfma_f32_16x16x32_bf16 v[136:139], v[204:207], v[74:77], v[136:139]
	v_mfma_f32_16x16x32_bf16 v[140:143], v[208:211], v[74:77], v[140:143]
	ds_read_b128 v[144:147], v125
	ds_read_b128 v[164:167], v126
	ds_read_b128 v[168:171], v127
	ds_read_b128 v[172:175], v128
	ds_read_b128 v[176:179], v129
	ds_read_b128 v[180:183], v130
	ds_read_b128 v[184:187], v131
	ds_read_b128 v[188:191], v132
	ds_read_b128 v[192:195], v112 offset:36864
	ds_read_b128 v[196:199], v112 offset:41472
	ds_read_b128 v[200:203], v112 offset:46080
	ds_read_b128 v[204:207], v112 offset:50688
	ds_read_b128 v[208:211], v112 offset:55296
	ds_read_b128 v[212:215], v112 offset:59904
	ds_read_b128 v[216:219], v112 offset:64512
	ds_read_b128 v[220:223], v113 offset:32256
	s_waitcnt lgkmcnt(14)
	v_cvt_pk_bf16_f32 v74, v160, v161
	v_cvt_pk_bf16_f32 v75, v162, v163
	s_nop 1
	v_mfma_f32_16x16x16_bf16 v[160:163], v[156:157], v[74:75], v[82:85]
	v_mfma_f32_16x16x16_bf16 v[86:89], v[158:159], v[74:75], v[86:89]
	v_mfma_f32_16x16x16_bf16 v[90:93], v[152:153], v[74:75], v[90:93]
	v_mfma_f32_16x16x16_bf16 v[70:73], v[154:155], v[74:75], v[70:73]
	v_mfma_f32_16x16x16_bf16 v[78:81], v[148:149], v[74:75], v[78:81]
	v_mfma_f32_16x16x16_bf16 v[136:139], v[150:151], v[74:75], v[136:139]
	v_mfma_f32_16x16x16_bf16 v[82:85], v[66:67], v[74:75], v[140:143]
	v_mfma_f32_16x16x16_bf16 v[74:77], v[68:69], v[74:75], v[62:65]
	s_nop 2
	v_exp_f32_e32 v240, v160
	v_exp_f32_e32 v241, v161
	v_exp_f32_e32 v242, v162
	v_exp_f32_e32 v243, v163
	v_pk_add_f32 v[240:241], v[240:241], 1.0 op_sel_hi:[1,0]
	v_pk_add_f32 v[242:243], v[242:243], 1.0 op_sel_hi:[1,0]
	v_rcp_f32_e32 v240, v240
	v_rcp_f32_e32 v241, v241
	v_rcp_f32_e32 v242, v242
	v_rcp_f32_e32 v243, v243
	v_pk_mul_f32 v[240:241], v[160:161], v[240:241]
	v_pk_mul_f32 v[242:243], v[162:163], v[242:243]
	v_cvt_pk_bf16_f32 v140, v240, v241
	v_cvt_pk_bf16_f32 v141, v242, v243
	v_exp_f32_e32 v244, v86
	v_exp_f32_e32 v245, v87
	v_exp_f32_e32 v246, v88
	v_exp_f32_e32 v247, v89
	v_pk_add_f32 v[244:245], v[244:245], 1.0 op_sel_hi:[1,0]
	v_pk_add_f32 v[246:247], v[246:247], 1.0 op_sel_hi:[1,0]
	v_rcp_f32_e32 v244, v244
	v_rcp_f32_e32 v245, v245
	v_rcp_f32_e32 v246, v246
	v_rcp_f32_e32 v247, v247
	v_pk_mul_f32 v[244:245], v[86:87], v[244:245]
	v_pk_mul_f32 v[246:247], v[88:89], v[246:247]
	v_cvt_pk_bf16_f32 v142, v244, v245
	v_cvt_pk_bf16_f32 v143, v246, v247
	v_mov_b32_e32 v236, v136
	v_mov_b32_e32 v237, v137
	v_mov_b32_e32 v238, v138
	v_mov_b32_e32 v239, v139
	ds_read_b128 v[248:251], v112 offset:36928
	ds_read_b128 v[136:139], v112 offset:41536
	ds_read_b128 v[152:155], v112 offset:46144
	ds_read_b128 v[156:159], v112 offset:50752
	ds_read_b128 v[160:163], v112 offset:55360
	ds_read_b128 v[224:227], v112 offset:59968
	ds_read_b128 v[228:231], v112 offset:64576
	ds_read_b128 v[232:235], v113 offset:32320
	ds_read_b128 v[62:65], v123
	ds_read_b128 v[66:69], v123 offset:64
	s_waitcnt lgkmcnt(14)
	v_mfma_f32_16x16x32_bf16 v[144:147], v[192:195], v[140:143], v[144:147]
	v_mfma_f32_16x16x32_bf16 v[164:167], v[196:199], v[140:143], v[164:167]
	v_mfma_f32_16x16x32_bf16 v[168:171], v[200:203], v[140:143], v[168:171]
	v_mfma_f32_16x16x32_bf16 v[172:175], v[204:207], v[140:143], v[172:175]
	s_waitcnt lgkmcnt(13)
	v_mfma_f32_16x16x32_bf16 v[176:179], v[208:211], v[140:143], v[176:179]
	s_waitcnt lgkmcnt(12)
	v_mfma_f32_16x16x32_bf16 v[180:183], v[212:215], v[140:143], v[180:183]
	s_waitcnt lgkmcnt(11)
	v_mfma_f32_16x16x32_bf16 v[184:187], v[216:219], v[140:143], v[184:187]
	s_waitcnt lgkmcnt(10)
	v_mfma_f32_16x16x32_bf16 v[140:143], v[220:223], v[140:143], v[188:191]
	v_exp_f32_e32 v240, v90
	v_exp_f32_e32 v241, v91
	v_exp_f32_e32 v242, v92
	v_exp_f32_e32 v243, v93
	v_pk_add_f32 v[240:241], v[240:241], 1.0 op_sel_hi:[1,0]
	v_pk_add_f32 v[242:243], v[242:243], 1.0 op_sel_hi:[1,0]
	v_rcp_f32_e32 v240, v240
	v_rcp_f32_e32 v241, v241
	v_rcp_f32_e32 v242, v242
	v_rcp_f32_e32 v243, v243
	v_pk_mul_f32 v[240:241], v[90:91], v[240:241]
	v_pk_mul_f32 v[242:243], v[92:93], v[242:243]
	v_cvt_pk_bf16_f32 v86, v240, v241
	v_cvt_pk_bf16_f32 v87, v242, v243
	v_exp_f32_e32 v244, v70
	v_exp_f32_e32 v245, v71
	v_exp_f32_e32 v246, v72
	v_exp_f32_e32 v247, v73
	v_pk_add_f32 v[244:245], v[244:245], 1.0 op_sel_hi:[1,0]
	v_pk_add_f32 v[246:247], v[246:247], 1.0 op_sel_hi:[1,0]
	v_rcp_f32_e32 v244, v244
	v_rcp_f32_e32 v245, v245
	v_rcp_f32_e32 v246, v246
	v_rcp_f32_e32 v247, v247
	v_pk_mul_f32 v[244:245], v[70:71], v[244:245]
	v_pk_mul_f32 v[246:247], v[72:73], v[246:247]
	v_cvt_pk_bf16_f32 v88, v244, v245
	v_cvt_pk_bf16_f32 v89, v246, v247
	s_nop 2
	ds_read_b128 v[188:191], v112 offset:36992
	ds_read_b128 v[192:195], v112 offset:41600
	ds_read_b128 v[196:199], v112 offset:46208
	ds_read_b128 v[200:203], v112 offset:50816
	ds_read_b128 v[204:207], v112 offset:55424
	ds_read_b128 v[208:211], v112 offset:60032
	ds_read_b128 v[212:215], v112 offset:64640
	ds_read_b128 v[216:219], v113 offset:32384
	ds_read_b128 v[70:73], v123 offset:128
	ds_read_b128 v[252:255], v123 offset:192
	s_waitcnt lgkmcnt(14)
	v_mfma_f32_16x16x32_bf16 v[144:147], v[248:251], v[86:89], v[144:147]
	v_mfma_f32_16x16x32_bf16 v[136:139], v[136:139], v[86:89], v[164:167]
	v_mfma_f32_16x16x32_bf16 v[152:155], v[152:155], v[86:89], v[168:171]
	v_mfma_f32_16x16x32_bf16 v[156:159], v[156:159], v[86:89], v[172:175]
	v_mfma_f32_16x16x32_bf16 v[160:163], v[160:163], v[86:89], v[176:179]
	v_mfma_f32_16x16x32_bf16 v[164:167], v[224:227], v[86:89], v[180:183]
	s_waitcnt lgkmcnt(13)
	v_mfma_f32_16x16x32_bf16 v[168:171], v[228:231], v[86:89], v[184:187]
	s_waitcnt lgkmcnt(12)
	v_mfma_f32_16x16x32_bf16 v[140:143], v[232:235], v[86:89], v[140:143]
	v_exp_f32_e32 v240, v78
	v_exp_f32_e32 v241, v79
	v_exp_f32_e32 v242, v80
	v_exp_f32_e32 v243, v81
	v_pk_add_f32 v[240:241], v[240:241], 1.0 op_sel_hi:[1,0]
	v_pk_add_f32 v[242:243], v[242:243], 1.0 op_sel_hi:[1,0]
	v_rcp_f32_e32 v240, v240
	v_rcp_f32_e32 v241, v241
	v_rcp_f32_e32 v242, v242
	v_rcp_f32_e32 v243, v243
	v_pk_mul_f32 v[240:241], v[78:79], v[240:241]
	v_pk_mul_f32 v[242:243], v[80:81], v[242:243]
	v_cvt_pk_bf16_f32 v148, v240, v241
	v_cvt_pk_bf16_f32 v149, v242, v243
	v_exp_f32_e32 v244, v236
	v_exp_f32_e32 v245, v237
	v_exp_f32_e32 v246, v238
	v_exp_f32_e32 v247, v239
	v_pk_add_f32 v[244:245], v[244:245], 1.0 op_sel_hi:[1,0]
	v_pk_add_f32 v[246:247], v[246:247], 1.0 op_sel_hi:[1,0]
	v_rcp_f32_e32 v244, v244
	v_rcp_f32_e32 v245, v245
	v_rcp_f32_e32 v246, v246
	v_rcp_f32_e32 v247, v247
	v_pk_mul_f32 v[244:245], v[236:237], v[244:245]
	v_pk_mul_f32 v[246:247], v[238:239], v[246:247]
	v_cvt_pk_bf16_f32 v150, v244, v245
	v_cvt_pk_bf16_f32 v151, v246, v247
	ds_read_b128 v[172:175], v112 offset:37056
	ds_read_b128 v[176:179], v112 offset:41664
	ds_read_b128 v[180:183], v112 offset:46272
	ds_read_b128 v[184:187], v112 offset:50880
	ds_read_b128 v[220:223], v112 offset:55488
	ds_read_b128 v[224:227], v112 offset:60096
	ds_read_b128 v[228:231], v112 offset:64704
	ds_read_b128 v[232:235], v113 offset:32448
	ds_read_b128 v[86:89], v123 offset:256
	ds_read_b128 v[90:93], v123 offset:320
	s_waitcnt lgkmcnt(14)
	v_mfma_f32_16x16x32_bf16 v[144:147], v[188:191], v[148:151], v[144:147]
	v_mfma_f32_16x16x32_bf16 v[136:139], v[192:195], v[148:151], v[136:139]
	v_mfma_f32_16x16x32_bf16 v[152:155], v[196:199], v[148:151], v[152:155]
	v_mfma_f32_16x16x32_bf16 v[156:159], v[200:203], v[148:151], v[156:159]
	v_mfma_f32_16x16x32_bf16 v[160:163], v[204:207], v[148:151], v[160:163]
	v_mfma_f32_16x16x32_bf16 v[164:167], v[208:211], v[148:151], v[164:167]
	s_waitcnt lgkmcnt(13)
	v_mfma_f32_16x16x32_bf16 v[168:171], v[212:215], v[148:151], v[168:171]
	s_waitcnt lgkmcnt(12)
	v_mfma_f32_16x16x32_bf16 v[140:143], v[216:219], v[148:151], v[140:143]
	v_exp_f32_e32 v148, v82
	v_exp_f32_e32 v149, v83
	v_exp_f32_e32 v150, v84
	v_exp_f32_e32 v151, v85
	v_add_f32_e32 v148, 1.0, v148
	v_add_f32_e32 v149, 1.0, v149
	v_rcp_f32_e32 v148, v148
	v_rcp_f32_e32 v149, v149
	v_add_f32_e32 v150, 1.0, v150
	v_add_f32_e32 v151, 1.0, v151
	v_rcp_f32_e32 v150, v150
	v_rcp_f32_e32 v151, v151
	v_pk_mul_f32 v[82:83], v[82:83], v[148:149]
	v_exp_f32_e32 v148, v74
	v_cvt_pk_bf16_f32 v82, v82, v83
	v_pk_mul_f32 v[84:85], v[84:85], v[150:151]
	v_exp_f32_e32 v149, v77
	v_cvt_pk_bf16_f32 v83, v84, v85
	v_exp_f32_e32 v85, v75
	v_add_f32_e32 v84, 1.0, v148
	v_exp_f32_e32 v148, v76
	v_rcp_f32_e32 v84, v84
	v_add_f32_e32 v85, 1.0, v85
	v_rcp_f32_e32 v85, v85
	v_add_f32_e32 v148, 1.0, v148
	v_rcp_f32_e32 v192, v148
	v_add_f32_e32 v148, 1.0, v149
	v_rcp_f32_e32 v193, v148
	ds_read_b128 v[148:151], v123 offset:384
	ds_read_b128 v[188:191], v123 offset:448
	v_pk_mul_f32 v[74:75], v[74:75], v[84:85]
	s_nop 0
	v_cvt_pk_bf16_f32 v84, v74, v75
	v_pk_mul_f32 v[74:75], v[76:77], v[192:193]
	s_nop 0
	v_cvt_pk_bf16_f32 v85, v74, v75
	s_waitcnt lgkmcnt(11)
	s_nop 0
	v_mfma_f32_16x16x32_bf16 v[74:77], v[172:175], v[82:85], v[144:147]
	s_waitcnt lgkmcnt(10)
	v_mfma_f32_16x16x32_bf16 v[136:139], v[176:179], v[82:85], v[136:139]
	s_waitcnt lgkmcnt(9)
	v_mfma_f32_16x16x32_bf16 v[144:147], v[180:183], v[82:85], v[152:155]
	s_waitcnt lgkmcnt(8)
	v_mfma_f32_16x16x32_bf16 v[152:155], v[184:187], v[82:85], v[156:159]
	s_waitcnt lgkmcnt(7)
	v_mfma_f32_16x16x32_bf16 v[156:159], v[220:223], v[82:85], v[160:163]
	s_waitcnt lgkmcnt(6)
	v_mfma_f32_16x16x32_bf16 v[160:163], v[224:227], v[82:85], v[164:167]
	s_waitcnt lgkmcnt(5)
	v_mfma_f32_16x16x32_bf16 v[164:167], v[228:231], v[82:85], v[168:171]
	s_waitcnt lgkmcnt(4)
	v_mfma_f32_16x16x32_bf16 v[82:85], v[232:235], v[82:85], v[140:143]
	s_nop 2
	v_exp_f32_e32 v140, v74
	v_exp_f32_e32 v141, v75
	v_exp_f32_e32 v168, v136
	v_exp_f32_e32 v169, v137
	v_exp_f32_e32 v170, v138
	v_exp_f32_e32 v171, v139
	v_exp_f32_e32 v142, v76
	v_exp_f32_e32 v143, v77
	v_add_f32_e32 v140, 1.0, v140
	v_add_f32_e32 v141, 1.0, v141
	v_rcp_f32_e32 v140, v140
	v_rcp_f32_e32 v141, v141
	v_add_f32_e32 v168, 1.0, v168
	v_add_f32_e32 v169, 1.0, v169
	v_rcp_f32_e32 v168, v168
	v_rcp_f32_e32 v169, v169
	v_pk_add_f32 v[170:171], v[170:171], 1.0 op_sel_hi:[1,0]
	v_pk_add_f32 v[142:143], v[142:143], 1.0 op_sel_hi:[1,0]
	v_rcp_f32_e32 v170, v170
	v_rcp_f32_e32 v171, v171
	v_rcp_f32_e32 v142, v142
	v_rcp_f32_e32 v143, v143
	v_exp_f32_e32 v172, v144
	v_exp_f32_e32 v173, v145
	v_pk_mul_f32 v[74:75], v[74:75], v[140:141]
	v_pk_mul_f32 v[136:137], v[136:137], v[168:169]
	v_pk_fma_f32 v[62:63], v[74:75], s[2:3], v[62:63] op_sel_hi:[1,0,1]
	v_exp_f32_e32 v174, v146
	v_pk_mul_f32 v[236:237], v[62:63], v[62:63]
	v_pk_add_f32 v[238:239], v[62:63], 0 op_sel_hi:[1,0]
	v_exp_f32_e32 v175, v147
	v_pk_fma_f32 v[66:67], v[136:137], s[2:3], v[66:67] op_sel_hi:[1,0,1]
	v_pk_mul_f32 v[136:137], v[138:139], v[170:171]
	v_pk_fma_f32 v[236:237], v[66:67], v[66:67], v[236:237]
	v_pk_add_f32 v[238:239], v[66:67], v[238:239]
	v_pk_fma_f32 v[68:69], v[136:137], s[2:3], v[68:69] op_sel_hi:[1,0,1]
	v_pk_mul_f32 v[74:75], v[76:77], v[142:143]
	v_pk_fma_f32 v[236:237], v[68:69], v[68:69], v[236:237]
	v_pk_add_f32 v[238:239], v[68:69], v[238:239]
	v_pk_add_f32 v[172:173], v[172:173], 1.0 op_sel_hi:[1,0]
	v_exp_f32_e32 v176, v152
	v_exp_f32_e32 v177, v153
	v_pk_fma_f32 v[64:65], v[74:75], s[2:3], v[64:65] op_sel_hi:[1,0,1]
	v_rcp_f32_e32 v172, v172
	v_pk_fma_f32 v[236:237], v[64:65], v[64:65], v[236:237]
	v_pk_add_f32 v[238:239], v[64:65], v[238:239]
	v_rcp_f32_e32 v173, v173
	v_pk_add_f32 v[174:175], v[174:175], 1.0 op_sel_hi:[1,0]
	v_exp_f32_e32 v178, v154
	v_exp_f32_e32 v179, v155
	v_rcp_f32_e32 v174, v174
	v_rcp_f32_e32 v175, v175
	v_pk_add_f32 v[176:177], v[176:177], 1.0 op_sel_hi:[1,0]
	v_exp_f32_e32 v180, v156
	v_exp_f32_e32 v181, v157
	v_rcp_f32_e32 v176, v176
	v_rcp_f32_e32 v177, v177
	v_pk_mul_f32 v[144:145], v[144:145], v[172:173]
	v_pk_add_f32 v[178:179], v[178:179], 1.0 op_sel_hi:[1,0]
	v_exp_f32_e32 v182, v158
	v_exp_f32_e32 v183, v159
	v_pk_fma_f32 v[70:71], v[144:145], s[2:3], v[70:71] op_sel_hi:[1,0,1]
	v_rcp_f32_e32 v178, v178
	v_pk_fma_f32 v[236:237], v[70:71], v[70:71], v[236:237]
	v_pk_add_f32 v[238:239], v[70:71], v[238:239]
	v_rcp_f32_e32 v179, v179
	v_pk_mul_f32 v[144:145], v[146:147], v[174:175]
	v_pk_add_f32 v[180:181], v[180:181], 1.0 op_sel_hi:[1,0]
	v_exp_f32_e32 v184, v160
	v_exp_f32_e32 v185, v161
	v_pk_fma_f32 v[72:73], v[144:145], s[2:3], v[72:73] op_sel_hi:[1,0,1]
	v_rcp_f32_e32 v180, v180
	v_pk_fma_f32 v[236:237], v[72:73], v[72:73], v[236:237]
	v_pk_add_f32 v[238:239], v[72:73], v[238:239]
	v_rcp_f32_e32 v181, v181
	v_pk_mul_f32 v[152:153], v[152:153], v[176:177]
	v_pk_add_f32 v[182:183], v[182:183], 1.0 op_sel_hi:[1,0]
	v_exp_f32_e32 v186, v162
	v_exp_f32_e32 v187, v163
	v_pk_fma_f32 v[78:79], v[152:153], s[2:3], v[252:253] op_sel_hi:[1,0,1]
	v_rcp_f32_e32 v182, v182
	v_pk_fma_f32 v[236:237], v[78:79], v[78:79], v[236:237]
	v_pk_add_f32 v[238:239], v[78:79], v[238:239]
	v_rcp_f32_e32 v183, v183
	v_pk_mul_f32 v[152:153], v[154:155], v[178:179]
	v_pk_add_f32 v[184:185], v[184:185], 1.0 op_sel_hi:[1,0]
	v_exp_f32_e32 v192, v164
	v_exp_f32_e32 v193, v165
	v_pk_fma_f32 v[80:81], v[152:153], s[2:3], v[254:255] op_sel_hi:[1,0,1]
	v_rcp_f32_e32 v184, v184
	v_pk_fma_f32 v[236:237], v[80:81], v[80:81], v[236:237]
	v_pk_add_f32 v[238:239], v[80:81], v[238:239]
	v_rcp_f32_e32 v185, v185
	v_pk_mul_f32 v[156:157], v[156:157], v[180:181]
	v_pk_add_f32 v[186:187], v[186:187], 1.0 op_sel_hi:[1,0]
	v_exp_f32_e32 v194, v166
	v_exp_f32_e32 v195, v167
	s_waitcnt lgkmcnt(3)
	v_pk_fma_f32 v[86:87], v[156:157], s[2:3], v[86:87] op_sel_hi:[1,0,1]
	v_rcp_f32_e32 v186, v186
	v_pk_fma_f32 v[236:237], v[86:87], v[86:87], v[236:237]
	v_pk_add_f32 v[238:239], v[86:87], v[238:239]
	v_rcp_f32_e32 v187, v187
	v_pk_mul_f32 v[156:157], v[158:159], v[182:183]
	v_pk_add_f32 v[192:193], v[192:193], 1.0 op_sel_hi:[1,0]
	v_exp_f32_e32 v196, v82
	v_exp_f32_e32 v197, v83
	v_pk_fma_f32 v[88:89], v[156:157], s[2:3], v[88:89] op_sel_hi:[1,0,1]
	v_rcp_f32_e32 v192, v192
	v_pk_fma_f32 v[236:237], v[88:89], v[88:89], v[236:237]
	v_pk_add_f32 v[238:239], v[88:89], v[238:239]
	v_rcp_f32_e32 v193, v193
	v_pk_mul_f32 v[160:161], v[160:161], v[184:185]
	v_pk_add_f32 v[194:195], v[194:195], 1.0 op_sel_hi:[1,0]
	v_exp_f32_e32 v198, v84
	v_exp_f32_e32 v199, v85
	s_waitcnt lgkmcnt(2)
	v_pk_fma_f32 v[90:91], v[160:161], s[2:3], v[90:91] op_sel_hi:[1,0,1]
	v_rcp_f32_e32 v194, v194
	v_pk_fma_f32 v[236:237], v[90:91], v[90:91], v[236:237]
	v_pk_add_f32 v[238:239], v[90:91], v[238:239]
	v_rcp_f32_e32 v195, v195
	v_pk_mul_f32 v[160:161], v[162:163], v[186:187]
	v_pk_add_f32 v[196:197], v[196:197], 1.0 op_sel_hi:[1,0]
	v_pk_fma_f32 v[92:93], v[160:161], s[2:3], v[92:93] op_sel_hi:[1,0,1]
	v_rcp_f32_e32 v196, v196
	v_pk_fma_f32 v[236:237], v[92:93], v[92:93], v[236:237]
	v_pk_add_f32 v[238:239], v[92:93], v[238:239]
	v_rcp_f32_e32 v197, v197
	v_pk_mul_f32 v[164:165], v[164:165], v[192:193]
	v_pk_add_f32 v[198:199], v[198:199], 1.0 op_sel_hi:[1,0]
	s_waitcnt lgkmcnt(1)
	v_pk_fma_f32 v[148:149], v[164:165], s[2:3], v[148:149] op_sel_hi:[1,0,1]
	v_rcp_f32_e32 v198, v198
	v_pk_fma_f32 v[236:237], v[148:149], v[148:149], v[236:237]
	v_pk_add_f32 v[238:239], v[148:149], v[238:239]
	v_rcp_f32_e32 v199, v199
	v_pk_mul_f32 v[164:165], v[166:167], v[194:195]
	s_nop 0
	v_pk_fma_f32 v[150:151], v[164:165], s[2:3], v[150:151] op_sel_hi:[1,0,1]
	v_pk_mul_f32 v[82:83], v[82:83], v[196:197]
	v_pk_fma_f32 v[236:237], v[150:151], v[150:151], v[236:237]
	v_pk_add_f32 v[238:239], v[150:151], v[238:239]
	s_waitcnt lgkmcnt(0)
	v_pk_fma_f32 v[82:83], v[82:83], s[2:3], v[188:189] op_sel_hi:[1,0,1]
	v_pk_mul_f32 v[84:85], v[84:85], v[198:199]
	v_pk_fma_f32 v[236:237], v[82:83], v[82:83], v[236:237]
	v_pk_fma_f32 v[84:85], v[84:85], s[2:3], v[190:191] op_sel_hi:[1,0,1]
	v_pk_add_f32 v[238:239], v[82:83], v[238:239]
	v_pk_fma_f32 v[236:237], v[84:85], v[84:85], v[236:237]
	v_pk_add_f32 v[238:239], v[84:85], v[238:239]
	v_add_f32_e32 v75, v236, v237
	v_add_f32_e32 v74, v238, v239
	s_nop 1
	v_permlane16_swap_b32_e32 v74, v75
	s_nop 0
	v_add_f32_e32 v74, v74, v75
	v_mov_b32_e32 v75, v74
	s_nop 1
	v_permlane32_swap_b32_e32 v74, v75
	s_nop 0
	v_add_f32_e32 v74, v74, v75
	v_mov_b32_e32 v75, v74
	s_nop 1
	v_permlane16_swap_b32_e32 v74, v75
	s_nop 0
	v_mul_f32_e32 v74, 0x3c000000, v74
	v_mul_f32_e32 v75, 0x3c000000, v75
	v_fma_f32 v75, -v74, v74, v75
	v_add_f32_e32 v75, 0x3727c5ac, v75
	v_rsq_f32_e32 v76, v75
	s_nop 0
	v_mul_f32_e64 v236, -v74, v76
	v_pk_fma_f32 v[62:63], v[62:63], v[76:77], v[236:237] op_sel_hi:[1,0,0]
	v_pk_fma_f32 v[64:65], v[64:65], v[76:77], v[236:237] op_sel_hi:[1,0,0]
	v_pk_fma_f32 v[66:67], v[66:67], v[76:77], v[236:237] op_sel_hi:[1,0,0]
	v_pk_fma_f32 v[68:69], v[68:69], v[76:77], v[236:237] op_sel_hi:[1,0,0]
	ds_write_b128 v123, v[62:65]
	v_pk_fma_f32 v[70:71], v[70:71], v[76:77], v[236:237] op_sel_hi:[1,0,0]
	v_pk_fma_f32 v[72:73], v[72:73], v[76:77], v[236:237] op_sel_hi:[1,0,0]
	ds_write_b128 v123, v[66:69] offset:64
	v_pk_fma_f32 v[78:79], v[78:79], v[76:77], v[236:237] op_sel_hi:[1,0,0]
	v_pk_fma_f32 v[80:81], v[80:81], v[76:77], v[236:237] op_sel_hi:[1,0,0]
	ds_write_b128 v123, v[70:73] offset:128
	v_pk_fma_f32 v[86:87], v[86:87], v[76:77], v[236:237] op_sel_hi:[1,0,0]
	v_pk_fma_f32 v[88:89], v[88:89], v[76:77], v[236:237] op_sel_hi:[1,0,0]
	ds_write_b128 v123, v[78:81] offset:192
	v_pk_fma_f32 v[90:91], v[90:91], v[76:77], v[236:237] op_sel_hi:[1,0,0]
	v_pk_fma_f32 v[92:93], v[92:93], v[76:77], v[236:237] op_sel_hi:[1,0,0]
	ds_write_b128 v123, v[86:89] offset:256
	v_pk_fma_f32 v[148:149], v[148:149], v[76:77], v[236:237] op_sel_hi:[1,0,0]
	v_pk_fma_f32 v[150:151], v[150:151], v[76:77], v[236:237] op_sel_hi:[1,0,0]
	ds_write_b128 v123, v[90:93] offset:320
	v_pk_fma_f32 v[82:83], v[82:83], v[76:77], v[236:237] op_sel_hi:[1,0,0]
	v_pk_fma_f32 v[84:85], v[84:85], v[76:77], v[236:237] op_sel_hi:[1,0,0]
	ds_write_b128 v123, v[148:151] offset:384
	ds_write_b128 v123, v[82:85] offset:448
	ds_read_b128 v[62:65], v121
	ds_read_b128 v[66:69], v121 offset:1088
	ds_read_b128 v[70:73], v121 offset:2176
	ds_read_b128 v[74:77], v121 offset:3264
	ds_read_b128 v[78:81], v121 offset:4352
	ds_read_b128 v[82:85], v121 offset:5440
	ds_read_b128 v[86:89], v121 offset:6528
	ds_read_b128 v[90:93], v121 offset:7616
	v_add_u32_e32 v136, 0xffffe400, v118
	s_waitcnt vmcnt(15) lgkmcnt(7)
	v_pk_fma_f32 v[64:65], v[56:57], v[64:65], v[60:61]
	v_pk_fma_f32 v[62:63], v[54:55], v[62:63], v[58:59]
	buffer_store_dwordx4 v[62:65], v136, s[4:7], 0 offen sc0 nt sc1
	v_cmp_lt_i32_e32 vcc, s8, v0
	s_or_b64 s[0:1], vcc, s[0:1]
	s_waitcnt lgkmcnt(6)
	v_pk_fma_f32 v[64:65], v[56:57], v[68:69], v[60:61]
	v_pk_fma_f32 v[62:63], v[54:55], v[66:67], v[58:59]
	v_add_u32_e32 v66, 0xffffe800, v118
	buffer_store_dwordx4 v[62:65], v66, s[4:7], 0 offen sc0 nt sc1
	v_add_u32_e32 v66, 0xffffec00, v118
	s_waitcnt lgkmcnt(5)
	v_pk_fma_f32 v[64:65], v[56:57], v[72:73], v[60:61]
	v_pk_fma_f32 v[62:63], v[54:55], v[70:71], v[58:59]
	buffer_store_dwordx4 v[62:65], v66, s[4:7], 0 offen sc0 nt sc1
	v_add_u32_e32 v66, 0xfffff000, v118
	s_waitcnt lgkmcnt(4)
	v_pk_fma_f32 v[64:65], v[56:57], v[76:77], v[60:61]
	v_pk_fma_f32 v[62:63], v[54:55], v[74:75], v[58:59]
	buffer_store_dwordx4 v[62:65], v66, s[4:7], 0 offen sc0 nt sc1
	v_add_u32_e32 v66, 0xfffff400, v118
	s_waitcnt lgkmcnt(3)
	v_pk_fma_f32 v[64:65], v[56:57], v[80:81], v[60:61]
	v_pk_fma_f32 v[62:63], v[54:55], v[78:79], v[58:59]
	buffer_store_dwordx4 v[62:65], v66, s[4:7], 0 offen sc0 nt sc1
	v_add_u32_e32 v66, 0xfffff800, v118
	s_waitcnt lgkmcnt(2)
	v_pk_fma_f32 v[64:65], v[56:57], v[84:85], v[60:61]
	v_pk_fma_f32 v[62:63], v[54:55], v[82:83], v[58:59]
	buffer_store_dwordx4 v[62:65], v66, s[4:7], 0 offen sc0 nt sc1
	v_add_u32_e32 v66, 0xfffffc00, v118
	s_waitcnt lgkmcnt(1)
	v_pk_fma_f32 v[64:65], v[56:57], v[88:89], v[60:61]
	v_pk_fma_f32 v[62:63], v[54:55], v[86:87], v[58:59]
	buffer_store_dwordx4 v[62:65], v66, s[4:7], 0 offen sc0 nt sc1
	s_waitcnt lgkmcnt(0)
	s_nop 0
	v_pk_fma_f32 v[64:65], v[56:57], v[92:93], v[60:61]
	v_pk_fma_f32 v[62:63], v[54:55], v[90:91], v[58:59]
	buffer_store_dwordx4 v[62:65], v118, s[4:7], 0 offen sc0 nt sc1
	v_add_u32_e32 v118, 0x1000000, v118
	s_nop 0
	v_mov_b32_e32 v62, v0
	s_waitcnt vmcnt(21)
	v_mov_b32_e32 v64, v135
	s_andn2_b64 exec, exec, s[0:1]
	s_cbranch_execnz .LBB1_6

	.amdhsa_kernel _Z9edge_mainPKfS0_PKiS2_PKcPcS0_S0_Pf
		.amdhsa_group_segment_fixed_size 156160
		.amdhsa_private_segment_fixed_size 0
		.amdhsa_kernarg_size 72
		.amdhsa_user_sgpr_count 2
		.amdhsa_user_sgpr_dispatch_ptr 0
		.amdhsa_user_sgpr_queue_ptr 0
		.amdhsa_user_sgpr_kernarg_segment_ptr 1
		.amdhsa_user_sgpr_dispatch_id 0
		.amdhsa_user_sgpr_kernarg_preload_length 0
		.amdhsa_user_sgpr_kernarg_preload_offset 0
		.amdhsa_user_sgpr_private_segment_size 0
		.amdhsa_uses_dynamic_stack 0
		.amdhsa_enable_private_segment 0
		.amdhsa_system_sgpr_workgroup_id_x 1
		.amdhsa_system_sgpr_workgroup_id_y 0
		.amdhsa_system_sgpr_workgroup_id_z 0
		.amdhsa_system_sgpr_workgroup_info 0
		.amdhsa_system_vgpr_workitem_id 0
		.amdhsa_next_free_vgpr 256
		.amdhsa_next_free_sgpr 96
		.amdhsa_accum_offset 256
		.amdhsa_reserve_vcc 1
		.amdhsa_float_round_mode_32 0
		.amdhsa_float_round_mode_16_64 0
		.amdhsa_float_denorm_mode_32 3
		.amdhsa_float_denorm_mode_16_64 3
		.amdhsa_dx10_clamp 1
		.amdhsa_ieee_mode 1
		.amdhsa_fp16_overflow 0
		.amdhsa_tg_split 0
		.amdhsa_exception_fp_ieee_invalid_op 0
		.amdhsa_exception_fp_denorm_src 0
		.amdhsa_exception_fp_ieee_div_zero 0
		.amdhsa_exception_fp_ieee_overflow 0
		.amdhsa_exception_fp_ieee_underflow 0
		.amdhsa_exception_fp_ieee_inexact 0
		.amdhsa_exception_int_div_zero 0
	.end_amdhsa_kernel

amdhsa.kernels:
  - .agpr_count:     0
    .args:
      - .actual_access:  read_only
        .address_space:  global
        .offset:         0
        .size:           8
        .value_kind:     global_buffer
      - .actual_access:  read_only
        .address_space:  global
        .offset:         8
        .size:           8
        .value_kind:     global_buffer
      - .actual_access:  read_only
        .address_space:  global
        .offset:         16
        .size:           8
        .value_kind:     global_buffer
      - .actual_access:  read_only
        .address_space:  global
        .offset:         24
        .size:           8
        .value_kind:     global_buffer
      - .actual_access:  read_only
        .address_space:  global
        .offset:         32
        .size:           8
        .value_kind:     global_buffer
      - .actual_access:  write_only
        .address_space:  global
        .offset:         40
        .size:           8
        .value_kind:     global_buffer
    .group_segment_fixed_size: 157696
    .kernarg_segment_align: 8
    .kernarg_segment_size: 48
    .language:       OpenCL C
    .language_version:
      - 2
      - 0
    .max_flat_workgroup_size: 512
    .name:           _Z4prepPKfS0_S0_S0_S0_Pc
    .private_segment_fixed_size: 0
    .sgpr_count:     36
    .sgpr_spill_count: 0
    .symbol:         _Z4prepPKfS0_S0_S0_S0_Pc.kd
    .uniform_work_group_size: 1
    .uses_dynamic_stack: false
    .vgpr_count:     256
    .vgpr_spill_count: 0
    .wavefront_size: 64
  - .agpr_count:     0
    .args:
      - .actual_access:  read_only
        .address_space:  global
        .offset:         0
        .size:           8
        .value_kind:     global_buffer
      - .actual_access:  read_only
        .address_space:  global
        .offset:         8
        .size:           8
        .value_kind:     global_buffer
      - .actual_access:  read_only
        .address_space:  global
        .offset:         16
        .size:           8
        .value_kind:     global_buffer
      - .actual_access:  read_only
        .address_space:  global
        .offset:         24
        .size:           8
        .value_kind:     global_buffer
      - .actual_access:  read_only
        .address_space:  global
        .offset:         32
        .size:           8
        .value_kind:     global_buffer
      - .actual_access:  write_only
        .address_space:  global
        .offset:         40
        .size:           8
        .value_kind:     global_buffer
      - .actual_access:  read_only
        .address_space:  global
        .offset:         48
        .size:           8
        .value_kind:     global_buffer
      - .actual_access:  read_only
        .address_space:  global
        .offset:         56
        .size:           8
        .value_kind:     global_buffer
      - .actual_access:  write_only
        .address_space:  global
        .offset:         64
        .size:           8
        .value_kind:     global_buffer
    .group_segment_fixed_size: 156160
    .kernarg_segment_align: 8
    .kernarg_segment_size: 72
    .language:       OpenCL C
    .language_version:
      - 2
      - 0
    .max_flat_workgroup_size: 512
    .name:           _Z9edge_mainPKfS0_PKiS2_PKcPcS0_S0_Pf
    .private_segment_fixed_size: 0
    .sgpr_count:     22
    .sgpr_spill_count: 0
    .symbol:         _Z9edge_mainPKfS0_PKiS2_PKcPcS0_S0_Pf.kd
    .uniform_work_group_size: 1
    .uses_dynamic_stack: false
    .vgpr_count:     256
    .vgpr_spill_count: 0
    .wavefront_size: 64
